# v6 + P5 out-proj epilogue (x1 = x + gate*acc): six residual loads kept in flight per wave in the free fragment registers instead of one load->wait->store round trip per 16-byte chunk
# baseline (speedup 1.0000x reference)
.LBB0_626:
	ds_read_b128 v[18:21], v188
	ds_read_b128 v[22:25], v188 offset:1024
	ds_read_b128 v[26:29], v188 offset:2048
	ds_read_b128 v[30:33], v188 offset:3072
	ds_read_b128 v[2:5], v189
	ds_read_b128 v[6:9], v189 offset:1024
	ds_read_b128 v[10:13], v189 offset:2048
	ds_read_b128 v[14:17], v189 offset:3072
	s_add_u32 s22, s20, 0xfffc0080
	s_addc_u32 s23, s21, -1
	s_cmp_eq_u32 s50, 12
	s_cselect_b32 s25, s13, s23
	s_cselect_b32 s24, s46, s22
	s_cselect_b32 s23, s11, s49
	s_cselect_b32 s22, s47, s48
	v_lshl_add_u64 v[174:175], s[20:21], 0, v[166:167]
	s_add_i32 m0, s19, 0xc000
	ds_read_b128 v[200:203], v190
	ds_read_b128 v[204:207], v190 offset:1024
	ds_read_b128 v[208:211], v190 offset:2048
	ds_read_b128 v[212:215], v190 offset:3072
	ds_read_b128 v[216:219], v190 offset:4096
	ds_read_b128 v[220:223], v190 offset:5120
	ds_read_b128 v[224:227], v190 offset:6144
	ds_read_b128 v[228:231], v190 offset:7168
	global_load_lds_dwordx4 v[174:175], off
	v_lshl_add_u64 v[174:175], s[20:21], 0, v[168:169]
	s_add_i32 m0, s19, 0xe000
	s_nop 0
	global_load_lds_dwordx4 v[174:175], off
	s_waitcnt vmcnt(8)
	s_waitcnt lgkmcnt(0)
	s_barrier
	s_setprio 1
	s_waitcnt lgkmcnt(0)
	v_mfma_scale_f32_16x16x128_f8f6f4 v[158:161], v[18:25], v[200:207], v[158:161], v191, v192 op_sel_hi:[0,0,0]
	v_mfma_scale_f32_16x16x128_f8f6f4 v[154:157], v[26:33], v[200:207], v[154:157], v191, v192 op_sel_hi:[0,0,0]
	v_mfma_scale_f32_16x16x128_f8f6f4 v[146:149], v[18:25], v[208:215], v[146:149], v191, v192 op_sel_hi:[0,0,0]
	v_mfma_scale_f32_16x16x128_f8f6f4 v[142:145], v[26:33], v[208:215], v[142:145], v191, v192 op_sel_hi:[0,0,0]
	v_mfma_scale_f32_16x16x128_f8f6f4 v[130:133], v[18:25], v[216:223], v[130:133], v191, v192 op_sel_hi:[0,0,0]
	v_mfma_scale_f32_16x16x128_f8f6f4 v[126:129], v[26:33], v[216:223], v[126:129], v191, v192 op_sel_hi:[0,0,0]
	v_mfma_scale_f32_16x16x128_f8f6f4 v[114:117], v[18:25], v[224:231], v[114:117], v191, v192 op_sel_hi:[0,0,0]
	v_mfma_scale_f32_16x16x128_f8f6f4 v[110:113], v[26:33], v[224:231], v[110:113], v191, v192 op_sel_hi:[0,0,0]
	s_setprio 0
	s_setprio 1
	v_mfma_scale_f32_16x16x128_f8f6f4 v[150:153], v[2:9], v[200:207], v[150:153], v191, v192 op_sel_hi:[0,0,0]
	v_mfma_scale_f32_16x16x128_f8f6f4 v[138:141], v[10:17], v[200:207], v[138:141], v191, v192 op_sel_hi:[0,0,0]
	v_mfma_scale_f32_16x16x128_f8f6f4 v[134:137], v[2:9], v[208:215], v[134:137], v191, v192 op_sel_hi:[0,0,0]
	v_mfma_scale_f32_16x16x128_f8f6f4 v[122:125], v[10:17], v[208:215], v[122:125], v191, v192 op_sel_hi:[0,0,0]
	v_mfma_scale_f32_16x16x128_f8f6f4 v[118:121], v[2:9], v[216:223], v[118:121], v191, v192 op_sel_hi:[0,0,0]
	v_mfma_scale_f32_16x16x128_f8f6f4 v[106:109], v[10:17], v[216:223], v[106:109], v191, v192 op_sel_hi:[0,0,0]
	v_mfma_scale_f32_16x16x128_f8f6f4 v[102:105], v[2:9], v[224:231], v[102:105], v191, v192 op_sel_hi:[0,0,0]
	v_mfma_scale_f32_16x16x128_f8f6f4 v[98:101], v[10:17], v[224:231], v[98:101], v191, v192 op_sel_hi:[0,0,0]
	s_setprio 0
	s_barrier
	s_add_i32 s51, s43, s33
	v_lshl_add_u64 v[174:175], s[22:23], 0, v[162:163]
	s_mov_b32 m0, s51
	ds_read_b128 v[200:203], v190 offset:16384
	ds_read_b128 v[204:207], v190 offset:17408
	ds_read_b128 v[208:211], v190 offset:18432
	ds_read_b128 v[212:215], v190 offset:19456
	ds_read_b128 v[216:219], v190 offset:20480
	ds_read_b128 v[220:223], v190 offset:21504
	ds_read_b128 v[224:227], v190 offset:22528
	ds_read_b128 v[228:231], v190 offset:23552
	global_load_lds_dwordx4 v[174:175], off
	s_add_i32 m0, s51, 0x2000
	s_add_u32 s52, s22, 0x40000
	v_lshl_add_u64 v[176:177], s[22:23], 0, v[164:165]
	s_addc_u32 s53, s23, 0
	s_add_i32 s51, s44, s33
	global_load_lds_dwordx4 v[176:177], off
	v_lshl_add_u64 v[184:185], s[52:53], 0, v[162:163]
	s_mov_b32 m0, s51
	v_lshl_add_u64 v[186:187], s[24:25], 0, v[164:165]
	global_load_lds_dwordx4 v[184:185], off
	v_lshl_add_u64 v[184:185], s[52:53], 0, v[164:165]
	s_add_i32 m0, s51, 0x2000
	s_nop 0
	global_load_lds_dwordx4 v[184:185], off
	v_lshl_add_u64 v[184:185], s[24:25], 0, v[162:163]
	s_mov_b32 m0, s19
	s_nop 0
	global_load_lds_dwordx4 v[184:185], off
	s_mov_b32 m0, s34
	s_nop 0
	global_load_lds_dwordx4 v[186:187], off
	s_waitcnt vmcnt(8)
	s_waitcnt lgkmcnt(0)
	s_barrier
	s_setprio 1
	s_waitcnt lgkmcnt(0)
	v_mfma_scale_f32_16x16x128_f8f6f4 v[94:97], v[18:25], v[200:207], v[94:97], v191, v192 op_sel_hi:[0,0,0]
	v_mfma_scale_f32_16x16x128_f8f6f4 v[90:93], v[26:33], v[200:207], v[90:93], v191, v192 op_sel_hi:[0,0,0]
	v_mfma_scale_f32_16x16x128_f8f6f4 v[82:85], v[18:25], v[208:215], v[82:85], v191, v192 op_sel_hi:[0,0,0]
	v_mfma_scale_f32_16x16x128_f8f6f4 v[78:81], v[26:33], v[208:215], v[78:81], v191, v192 op_sel_hi:[0,0,0]
	v_mfma_scale_f32_16x16x128_f8f6f4 v[66:69], v[18:25], v[216:223], v[66:69], v191, v192 op_sel_hi:[0,0,0]
	v_mfma_scale_f32_16x16x128_f8f6f4 v[62:65], v[26:33], v[216:223], v[62:65], v191, v192 op_sel_hi:[0,0,0]
	v_mfma_scale_f32_16x16x128_f8f6f4 v[50:53], v[18:25], v[224:231], v[50:53], v191, v192 op_sel_hi:[0,0,0]
	v_mfma_scale_f32_16x16x128_f8f6f4 v[46:49], v[26:33], v[224:231], v[46:49], v191, v192 op_sel_hi:[0,0,0]
	s_setprio 0
	s_setprio 1
	v_mfma_scale_f32_16x16x128_f8f6f4 v[86:89], v[2:9], v[200:207], v[86:89], v191, v192 op_sel_hi:[0,0,0]
	v_mfma_scale_f32_16x16x128_f8f6f4 v[74:77], v[10:17], v[200:207], v[74:77], v191, v192 op_sel_hi:[0,0,0]
	v_mfma_scale_f32_16x16x128_f8f6f4 v[70:73], v[2:9], v[208:215], v[70:73], v191, v192 op_sel_hi:[0,0,0]
	v_mfma_scale_f32_16x16x128_f8f6f4 v[58:61], v[10:17], v[208:215], v[58:61], v191, v192 op_sel_hi:[0,0,0]
	v_mfma_scale_f32_16x16x128_f8f6f4 v[54:57], v[2:9], v[216:223], v[54:57], v191, v192 op_sel_hi:[0,0,0]
	v_mfma_scale_f32_16x16x128_f8f6f4 v[42:45], v[10:17], v[216:223], v[42:45], v191, v192 op_sel_hi:[0,0,0]
	v_mfma_scale_f32_16x16x128_f8f6f4 v[38:41], v[2:9], v[224:231], v[38:41], v191, v192 op_sel_hi:[0,0,0]
	v_mfma_scale_f32_16x16x128_f8f6f4 v[34:37], v[10:17], v[224:231], v[34:37], v191, v192 op_sel_hi:[0,0,0]
	s_setprio 0
	s_barrier
	s_add_i32 s51, 0, 0x18000
	s_add_i32 s52, 0, 0x1c000
	v_add_u32_e32 v14, s51, v181
	v_add_u32_e32 v30, s52, v181
	ds_read_b128 v[2:5], v14
	ds_read_b128 v[6:9], v14 offset:1024
	ds_read_b128 v[10:13], v14 offset:2048
	ds_read_b128 v[14:17], v14 offset:3072
	ds_read_b128 v[18:21], v30
	ds_read_b128 v[22:25], v30 offset:1024
	ds_read_b128 v[26:29], v30 offset:2048
	ds_read_b128 v[30:33], v30 offset:3072
	s_add_u32 s24, s24, 0x40000
	s_addc_u32 s25, s25, 0
	s_mov_b32 m0, s35
	v_lshl_add_u64 v[232:233], s[24:25], 0, v[162:163]
	ds_read_b128 v[200:203], v190 offset:32768
	ds_read_b128 v[204:207], v190 offset:33792
	ds_read_b128 v[208:211], v190 offset:34816
	ds_read_b128 v[212:215], v190 offset:35840
	ds_read_b128 v[216:219], v190 offset:36864
	ds_read_b128 v[220:223], v190 offset:37888
	ds_read_b128 v[224:227], v190 offset:38912
	ds_read_b128 v[228:231], v190 offset:39936
	global_load_lds_dwordx4 v[232:233], off
	v_lshl_add_u64 v[232:233], s[24:25], 0, v[164:165]
	s_mov_b32 m0, s36
	s_nop 0
	global_load_lds_dwordx4 v[232:233], off
	s_waitcnt vmcnt(8)
	s_waitcnt lgkmcnt(0)
	s_barrier
	s_setprio 1
	s_waitcnt lgkmcnt(0)
	v_mfma_scale_f32_16x16x128_f8f6f4 v[158:161], v[2:9], v[200:207], v[158:161], v191, v192 op_sel_hi:[0,0,0]
	v_mfma_scale_f32_16x16x128_f8f6f4 v[154:157], v[10:17], v[200:207], v[154:157], v191, v192 op_sel_hi:[0,0,0]
	v_mfma_scale_f32_16x16x128_f8f6f4 v[146:149], v[2:9], v[208:215], v[146:149], v191, v192 op_sel_hi:[0,0,0]
	v_mfma_scale_f32_16x16x128_f8f6f4 v[142:145], v[10:17], v[208:215], v[142:145], v191, v192 op_sel_hi:[0,0,0]
	v_mfma_scale_f32_16x16x128_f8f6f4 v[130:133], v[2:9], v[216:223], v[130:133], v191, v192 op_sel_hi:[0,0,0]
	v_mfma_scale_f32_16x16x128_f8f6f4 v[126:129], v[10:17], v[216:223], v[126:129], v191, v192 op_sel_hi:[0,0,0]
	v_mfma_scale_f32_16x16x128_f8f6f4 v[114:117], v[2:9], v[224:231], v[114:117], v191, v192 op_sel_hi:[0,0,0]
	v_mfma_scale_f32_16x16x128_f8f6f4 v[110:113], v[10:17], v[224:231], v[110:113], v191, v192 op_sel_hi:[0,0,0]
	s_setprio 0
	s_setprio 1
	v_mfma_scale_f32_16x16x128_f8f6f4 v[150:153], v[18:25], v[200:207], v[150:153], v191, v192 op_sel_hi:[0,0,0]
	v_mfma_scale_f32_16x16x128_f8f6f4 v[138:141], v[26:33], v[200:207], v[138:141], v191, v192 op_sel_hi:[0,0,0]
	v_mfma_scale_f32_16x16x128_f8f6f4 v[134:137], v[18:25], v[208:215], v[134:137], v191, v192 op_sel_hi:[0,0,0]
	v_mfma_scale_f32_16x16x128_f8f6f4 v[122:125], v[26:33], v[208:215], v[122:125], v191, v192 op_sel_hi:[0,0,0]
	v_mfma_scale_f32_16x16x128_f8f6f4 v[118:121], v[18:25], v[216:223], v[118:121], v191, v192 op_sel_hi:[0,0,0]
	v_mfma_scale_f32_16x16x128_f8f6f4 v[106:109], v[26:33], v[216:223], v[106:109], v191, v192 op_sel_hi:[0,0,0]
	v_mfma_scale_f32_16x16x128_f8f6f4 v[102:105], v[18:25], v[224:231], v[102:105], v191, v192 op_sel_hi:[0,0,0]
	v_mfma_scale_f32_16x16x128_f8f6f4 v[98:101], v[26:33], v[224:231], v[98:101], v191, v192 op_sel_hi:[0,0,0]
	s_setprio 0
	s_barrier
	s_add_i32 s24, s51, s33
	v_lshl_add_u64 v[174:175], v[174:175], 0, s[4:5]
	s_mov_b32 m0, s24
	ds_read_b128 v[200:203], v190 offset:49152
	ds_read_b128 v[204:207], v190 offset:50176
	ds_read_b128 v[208:211], v190 offset:51200
	ds_read_b128 v[212:215], v190 offset:52224
	ds_read_b128 v[216:219], v190 offset:53248
	ds_read_b128 v[220:223], v190 offset:54272
	ds_read_b128 v[224:227], v190 offset:55296
	ds_read_b128 v[228:231], v190 offset:56320
	global_load_lds_dwordx4 v[174:175], off
	s_add_i32 m0, s24, 0x2000
	s_add_u32 s22, s22, 0x40080
	v_lshl_add_u64 v[174:175], v[176:177], 0, s[4:5]
	s_addc_u32 s23, s23, 0
	s_add_i32 s24, s52, s33
	global_load_lds_dwordx4 v[174:175], off
	v_lshl_add_u64 v[174:175], s[22:23], 0, v[162:163]
	s_mov_b32 m0, s24
	s_nop 0
	global_load_lds_dwordx4 v[174:175], off
	v_lshl_add_u64 v[174:175], s[22:23], 0, v[164:165]
	s_add_i32 m0, s24, 0x2000
	s_nop 0
	global_load_lds_dwordx4 v[174:175], off
	v_lshl_add_u64 v[174:175], v[184:185], 0, s[4:5]
	s_mov_b32 m0, s40
	s_nop 0
	global_load_lds_dwordx4 v[174:175], off
	v_lshl_add_u64 v[174:175], v[186:187], 0, s[4:5]
	s_mov_b32 m0, s41
	s_nop 0
	global_load_lds_dwordx4 v[174:175], off
	s_waitcnt vmcnt(8)
	s_waitcnt lgkmcnt(0)
	s_barrier
	s_setprio 1
	s_waitcnt lgkmcnt(0)
	v_mfma_scale_f32_16x16x128_f8f6f4 v[94:97], v[2:9], v[200:207], v[94:97], v191, v192 op_sel_hi:[0,0,0]
	v_mfma_scale_f32_16x16x128_f8f6f4 v[90:93], v[10:17], v[200:207], v[90:93], v191, v192 op_sel_hi:[0,0,0]
	v_mfma_scale_f32_16x16x128_f8f6f4 v[82:85], v[2:9], v[208:215], v[82:85], v191, v192 op_sel_hi:[0,0,0]
	v_mfma_scale_f32_16x16x128_f8f6f4 v[78:81], v[10:17], v[208:215], v[78:81], v191, v192 op_sel_hi:[0,0,0]
	v_mfma_scale_f32_16x16x128_f8f6f4 v[66:69], v[2:9], v[216:223], v[66:69], v191, v192 op_sel_hi:[0,0,0]
	v_mfma_scale_f32_16x16x128_f8f6f4 v[62:65], v[10:17], v[216:223], v[62:65], v191, v192 op_sel_hi:[0,0,0]
	v_mfma_scale_f32_16x16x128_f8f6f4 v[50:53], v[2:9], v[224:231], v[50:53], v191, v192 op_sel_hi:[0,0,0]
	v_mfma_scale_f32_16x16x128_f8f6f4 v[46:49], v[10:17], v[224:231], v[46:49], v191, v192 op_sel_hi:[0,0,0]
	s_setprio 0
	s_setprio 1
	v_mfma_scale_f32_16x16x128_f8f6f4 v[86:89], v[18:25], v[200:207], v[86:89], v191, v192 op_sel_hi:[0,0,0]
	v_mfma_scale_f32_16x16x128_f8f6f4 v[74:77], v[26:33], v[200:207], v[74:77], v191, v192 op_sel_hi:[0,0,0]
	v_mfma_scale_f32_16x16x128_f8f6f4 v[70:73], v[18:25], v[208:215], v[70:73], v191, v192 op_sel_hi:[0,0,0]
	v_mfma_scale_f32_16x16x128_f8f6f4 v[58:61], v[26:33], v[208:215], v[58:61], v191, v192 op_sel_hi:[0,0,0]
	v_mfma_scale_f32_16x16x128_f8f6f4 v[54:57], v[18:25], v[216:223], v[54:57], v191, v192 op_sel_hi:[0,0,0]
	v_mfma_scale_f32_16x16x128_f8f6f4 v[42:45], v[26:33], v[216:223], v[42:45], v191, v192 op_sel_hi:[0,0,0]
	v_mfma_scale_f32_16x16x128_f8f6f4 v[38:41], v[18:25], v[224:231], v[38:41], v191, v192 op_sel_hi:[0,0,0]
	v_mfma_scale_f32_16x16x128_f8f6f4 v[34:37], v[26:33], v[224:231], v[34:37], v191, v192 op_sel_hi:[0,0,0]
	s_setprio 0
	s_barrier
	s_add_i32 s50, s50, 2
	s_add_u32 s20, s20, 0x100
	s_addc_u32 s21, s21, 0
	s_add_u32 s48, s48, 0x100
	s_addc_u32 s49, s49, 0
	s_cmp_gt_u32 s50, 13
	s_cbranch_scc0 .LBB0_626
	v_lshl_add_u32 v26, s18, 8, v1
	v_lshl_or_b32 v24, s45, 8, v183
	s_ashr_i32 s11, s18, 3
	v_ashrrev_i32_e32 v27, 31, v26
	s_mul_hi_i32 s13, s11, 0x1c000
	s_mul_i32 s11, s11, 0x1c000
	v_ashrrev_i32_e32 v25, 31, v24
	v_lshlrev_b64 v[4:5], 11, v[26:27]
	s_add_u32 s20, s38, s11
	v_lshl_add_u64 v[4:5], v[4:5], 0, v[24:25]
	v_readlane_b32 s48, v250, 56
	s_addc_u32 s21, s39, s13
	v_lshlrev_b64 v[18:19], 2, v[4:5]
	v_readlane_b32 s49, v250, 57
	s_nop 15
	s_nop 15
	v_lshl_add_u64 v[2:3], v[24:25], 2, s[20:21]
	v_lshl_add_u64 v[30:31], s[76:77], 0, v[18:19]
	v_lshl_add_u64 v[28:29], s[48:49], 0, v[18:19]
	global_load_dwordx4 v[14:17], v[2:3], off
	global_load_dwordx4 v[10:13], v[2:3], off offset:64
	global_load_dwordx4 v[6:9], v[2:3], off offset:512
	s_nop 0
	global_load_dwordx4 v[2:5], v[2:3], off offset:576
	v_mov_b32_e32 v24, v18
	v_add_u32_e32 v25, 0x20000, v18
	v_add_u32_e32 v26, 0x40000, v18
	v_add_u32_e32 v27, 0x60000, v18
	v_add_u32_e32 v28, 0x100000, v18
	v_add_u32_e32 v29, 0x120000, v18
	v_add_u32_e32 v30, 0x140000, v18
	v_add_u32_e32 v31, 0x160000, v18
	global_load_dwordx4 v[200:203], v24, s[48:49]
	global_load_dwordx4 v[204:207], v24, s[48:49] offset:64
	global_load_dwordx4 v[208:211], v24, s[48:49] offset:512
	global_load_dwordx4 v[212:215], v24, s[48:49] offset:576
	global_load_dwordx4 v[216:219], v25, s[48:49]
	global_load_dwordx4 v[220:223], v25, s[48:49] offset:64
	s_mov_b64 s[20:21], 0x100000
	v_readlane_b32 s60, v251, 4
	v_readlane_b32 s61, v251, 5
	v_readlane_b32 s62, v251, 6
	v_readlane_b32 s63, v251, 7
	s_mov_b32 s45, s10
	s_mov_b32 s18, s12
	s_and_b64 vcc, exec, s[0:1]
	s_mov_b64 s[22:23], s[16:17]
	v_readlane_b32 s50, v250, 58
	v_readlane_b32 s51, v250, 59
	v_readlane_b32 s52, v250, 60
	v_readlane_b32 s53, v250, 61
	v_readlane_b32 s54, v250, 62
	v_readlane_b32 s55, v250, 63
	v_readlane_b32 s56, v251, 0
	v_readlane_b32 s57, v251, 1
	v_readlane_b32 s58, v251, 2
	v_readlane_b32 s59, v251, 3
	s_mov_b64 s[20:21], 0x120000
	s_mov_b64 s[20:21], s[14:15]
	s_waitcnt vmcnt(5)
	v_pk_fma_f32 v[202:203], v[160:161], v[16:17], v[202:203]
	v_pk_fma_f32 v[200:201], v[158:159], v[14:15], v[200:201]
	global_store_dwordx4 v24, v[200:203], s[76:77]
	global_load_dwordx4 v[224:227], v25, s[48:49] offset:512
	s_waitcnt vmcnt(6)
	v_pk_fma_f32 v[206:207], v[156:157], v[12:13], v[206:207]
	v_pk_fma_f32 v[204:205], v[154:155], v[10:11], v[204:205]
	global_store_dwordx4 v24, v[204:207], s[76:77] offset:64
	global_load_dwordx4 v[228:231], v25, s[48:49] offset:576
	s_waitcnt vmcnt(7)
	v_pk_fma_f32 v[210:211], v[152:153], v[8:9], v[210:211]
	v_pk_fma_f32 v[208:209], v[150:151], v[6:7], v[208:209]
	global_store_dwordx4 v24, v[208:211], s[76:77] offset:512
	global_load_dwordx4 v[200:203], v26, s[48:49]
	s_waitcnt vmcnt(8)
	v_pk_fma_f32 v[214:215], v[140:141], v[4:5], v[214:215]
	v_pk_fma_f32 v[212:213], v[138:139], v[2:3], v[212:213]
	global_store_dwordx4 v24, v[212:215], s[76:77] offset:576
	global_load_dwordx4 v[204:207], v26, s[48:49] offset:64
	s_waitcnt vmcnt(9)
	v_pk_fma_f32 v[218:219], v[148:149], v[16:17], v[218:219]
	v_pk_fma_f32 v[216:217], v[146:147], v[14:15], v[216:217]
	global_store_dwordx4 v25, v[216:219], s[76:77]
	global_load_dwordx4 v[208:211], v26, s[48:49] offset:512
	s_waitcnt vmcnt(10)
	v_pk_fma_f32 v[222:223], v[144:145], v[12:13], v[222:223]
	v_pk_fma_f32 v[220:221], v[142:143], v[10:11], v[220:221]
	global_store_dwordx4 v25, v[220:223], s[76:77] offset:64
	global_load_dwordx4 v[212:215], v26, s[48:49] offset:576
	s_waitcnt vmcnt(10)
	v_pk_fma_f32 v[226:227], v[136:137], v[8:9], v[226:227]
	v_pk_fma_f32 v[224:225], v[134:135], v[6:7], v[224:225]
	global_store_dwordx4 v25, v[224:227], s[76:77] offset:512
	global_load_dwordx4 v[216:219], v27, s[48:49]
	s_waitcnt vmcnt(10)
	v_pk_fma_f32 v[230:231], v[124:125], v[4:5], v[230:231]
	v_pk_fma_f32 v[228:229], v[122:123], v[2:3], v[228:229]
	global_store_dwordx4 v25, v[228:231], s[76:77] offset:576
	global_load_dwordx4 v[220:223], v27, s[48:49] offset:64
	s_waitcnt vmcnt(10)
	v_pk_fma_f32 v[202:203], v[132:133], v[16:17], v[202:203]
	v_pk_fma_f32 v[200:201], v[130:131], v[14:15], v[200:201]
	global_store_dwordx4 v26, v[200:203], s[76:77]
	global_load_dwordx4 v[224:227], v27, s[48:49] offset:512
	s_waitcnt vmcnt(10)
	v_pk_fma_f32 v[206:207], v[128:129], v[12:13], v[206:207]
	v_pk_fma_f32 v[204:205], v[126:127], v[10:11], v[204:205]
	global_store_dwordx4 v26, v[204:207], s[76:77] offset:64
	global_load_dwordx4 v[228:231], v27, s[48:49] offset:576
	s_waitcnt vmcnt(10)
	v_pk_fma_f32 v[210:211], v[120:121], v[8:9], v[210:211]
	v_pk_fma_f32 v[208:209], v[118:119], v[6:7], v[208:209]
	global_store_dwordx4 v26, v[208:211], s[76:77] offset:512
	global_load_dwordx4 v[200:203], v28, s[48:49]
	s_waitcnt vmcnt(10)
	v_pk_fma_f32 v[214:215], v[108:109], v[4:5], v[214:215]
	v_pk_fma_f32 v[212:213], v[106:107], v[2:3], v[212:213]
	global_store_dwordx4 v26, v[212:215], s[76:77] offset:576
	global_load_dwordx4 v[204:207], v28, s[48:49] offset:64
	s_waitcnt vmcnt(10)
	v_pk_fma_f32 v[218:219], v[116:117], v[16:17], v[218:219]
	v_pk_fma_f32 v[216:217], v[114:115], v[14:15], v[216:217]
	global_store_dwordx4 v27, v[216:219], s[76:77]
	global_load_dwordx4 v[208:211], v28, s[48:49] offset:512
	s_waitcnt vmcnt(10)
	v_pk_fma_f32 v[222:223], v[112:113], v[12:13], v[222:223]
	v_pk_fma_f32 v[220:221], v[110:111], v[10:11], v[220:221]
	global_store_dwordx4 v27, v[220:223], s[76:77] offset:64
	global_load_dwordx4 v[212:215], v28, s[48:49] offset:576
	s_waitcnt vmcnt(10)
	v_pk_fma_f32 v[226:227], v[104:105], v[8:9], v[226:227]
	v_pk_fma_f32 v[224:225], v[102:103], v[6:7], v[224:225]
	global_store_dwordx4 v27, v[224:227], s[76:77] offset:512
	global_load_dwordx4 v[216:219], v29, s[48:49]
	s_waitcnt vmcnt(10)
	v_pk_fma_f32 v[230:231], v[100:101], v[4:5], v[230:231]
	v_pk_fma_f32 v[228:229], v[98:99], v[2:3], v[228:229]
	global_store_dwordx4 v27, v[228:231], s[76:77] offset:576
	global_load_dwordx4 v[220:223], v29, s[48:49] offset:64
	s_waitcnt vmcnt(10)
	v_pk_fma_f32 v[202:203], v[96:97], v[16:17], v[202:203]
	v_pk_fma_f32 v[200:201], v[94:95], v[14:15], v[200:201]
	global_store_dwordx4 v28, v[200:203], s[76:77]
	global_load_dwordx4 v[224:227], v29, s[48:49] offset:512
	s_waitcnt vmcnt(10)
	v_pk_fma_f32 v[206:207], v[92:93], v[12:13], v[206:207]
	v_pk_fma_f32 v[204:205], v[90:91], v[10:11], v[204:205]
	global_store_dwordx4 v28, v[204:207], s[76:77] offset:64
	global_load_dwordx4 v[228:231], v29, s[48:49] offset:576
	s_waitcnt vmcnt(10)
	v_pk_fma_f32 v[210:211], v[88:89], v[8:9], v[210:211]
	v_pk_fma_f32 v[208:209], v[86:87], v[6:7], v[208:209]
	global_store_dwordx4 v28, v[208:211], s[76:77] offset:512
	global_load_dwordx4 v[200:203], v30, s[48:49]
	s_waitcnt vmcnt(10)
	v_pk_fma_f32 v[214:215], v[76:77], v[4:5], v[214:215]
	v_pk_fma_f32 v[212:213], v[74:75], v[2:3], v[212:213]
	global_store_dwordx4 v28, v[212:215], s[76:77] offset:576
	global_load_dwordx4 v[204:207], v30, s[48:49] offset:64
	s_waitcnt vmcnt(10)
	v_pk_fma_f32 v[218:219], v[84:85], v[16:17], v[218:219]
	v_pk_fma_f32 v[216:217], v[82:83], v[14:15], v[216:217]
	global_store_dwordx4 v29, v[216:219], s[76:77]
	global_load_dwordx4 v[208:211], v30, s[48:49] offset:512
	s_waitcnt vmcnt(10)
	v_pk_fma_f32 v[222:223], v[80:81], v[12:13], v[222:223]
	v_pk_fma_f32 v[220:221], v[78:79], v[10:11], v[220:221]
	global_store_dwordx4 v29, v[220:223], s[76:77] offset:64
	global_load_dwordx4 v[212:215], v30, s[48:49] offset:576
	s_waitcnt vmcnt(10)
	v_pk_fma_f32 v[226:227], v[72:73], v[8:9], v[226:227]
	v_pk_fma_f32 v[224:225], v[70:71], v[6:7], v[224:225]
	global_store_dwordx4 v29, v[224:227], s[76:77] offset:512
	global_load_dwordx4 v[216:219], v31, s[48:49]
	s_waitcnt vmcnt(10)
	v_pk_fma_f32 v[230:231], v[60:61], v[4:5], v[230:231]
	v_pk_fma_f32 v[228:229], v[58:59], v[2:3], v[228:229]
	global_store_dwordx4 v29, v[228:231], s[76:77] offset:576
	global_load_dwordx4 v[220:223], v31, s[48:49] offset:64
	s_waitcnt vmcnt(10)
	v_pk_fma_f32 v[202:203], v[68:69], v[16:17], v[202:203]
	v_pk_fma_f32 v[200:201], v[66:67], v[14:15], v[200:201]
	global_store_dwordx4 v30, v[200:203], s[76:77]
	global_load_dwordx4 v[224:227], v31, s[48:49] offset:512
	s_waitcnt vmcnt(10)
	v_pk_fma_f32 v[206:207], v[64:65], v[12:13], v[206:207]
	v_pk_fma_f32 v[204:205], v[62:63], v[10:11], v[204:205]
	global_store_dwordx4 v30, v[204:207], s[76:77] offset:64
	global_load_dwordx4 v[228:231], v31, s[48:49] offset:576
	s_waitcnt vmcnt(10)
	v_pk_fma_f32 v[210:211], v[56:57], v[8:9], v[210:211]
	v_pk_fma_f32 v[208:209], v[54:55], v[6:7], v[208:209]
	global_store_dwordx4 v30, v[208:211], s[76:77] offset:512
	s_waitcnt vmcnt(9)
	v_pk_fma_f32 v[214:215], v[44:45], v[4:5], v[214:215]
	v_pk_fma_f32 v[212:213], v[42:43], v[2:3], v[212:213]
	global_store_dwordx4 v30, v[212:215], s[76:77] offset:576
	s_waitcnt vmcnt(8)
	v_pk_fma_f32 v[218:219], v[52:53], v[16:17], v[218:219]
	v_pk_fma_f32 v[216:217], v[50:51], v[14:15], v[216:217]
	global_store_dwordx4 v31, v[216:219], s[76:77]
	s_waitcnt vmcnt(7)
	v_pk_fma_f32 v[222:223], v[48:49], v[12:13], v[222:223]
	v_pk_fma_f32 v[220:221], v[46:47], v[10:11], v[220:221]
	global_store_dwordx4 v31, v[220:223], s[76:77] offset:64
	s_waitcnt vmcnt(6)
	v_pk_fma_f32 v[226:227], v[40:41], v[8:9], v[226:227]
	v_pk_fma_f32 v[224:225], v[38:39], v[6:7], v[224:225]
	global_store_dwordx4 v31, v[224:227], s[76:77] offset:512
	s_waitcnt vmcnt(5)
	v_pk_fma_f32 v[230:231], v[36:37], v[4:5], v[230:231]
	v_pk_fma_f32 v[228:229], v[34:35], v[2:3], v[228:229]
	global_store_dwordx4 v31, v[228:231], s[76:77] offset:576
	s_cbranch_vccz .LBB0_619
	s_waitcnt vmcnt(0)
	s_cmpk_gt_u32 s26, 0xff
	s_cbranch_scc1 .LBB0_630
	s_barrier
